# P3 mLSTM scan: chunk-state (DC) loads of batch k+1 prefetched before batch k is computed (16 extra VGPRs), vmcnt counts re-derived
# speedup vs baseline: 1.0092x; 1.0092x over previous
; __device__ __forceinline__ void p3_mlstm_scan(const Params& P, int tid, int vb) {
;     const unsigned* __restrict__ DC = (const unsigned*)((unsigned char*)P.out + OUT_DC); unsigned* __restrict__ CS = (unsigned*)((unsigned char*)P.out + OUT_CS);
;     const float* __restrict__ DN = (const float*)(P.ws + WS_DN); float* __restrict__ NS = (float*)(P.ws + WS_NS); float* SC = (float*)(P.ws + WS_SC);
;     for (int gid = vb * 512 + tid; gid < 8 * 8192; gid += gridDim.x * 512) {
;         const int bh = gid >> 13, idx = gid & 8191; const bool hasn = idx < 64;
;         float C0 = 0.f, C1 = 0.f, n0 = 0.f, n1 = 0.f, m = 0.f;
;         for (int j0 = 0; j0 < 256; j0 += 16) {
.LBB0_580:
	v_lshl_or_b32 v1, s72, 9, v0
	s_mov_b32 s0, 0x10000
	v_cmp_gt_i32_e32 vcc, s0, v1
	s_and_saveexec_b64 s[12:13], vcc
	s_cbranch_execz .LBB0_681
	s_load_dwordx4 s[4:7], s[94:95], 0xa0
	s_lshl_b32 s10, s68, 9
	s_waitcnt vmcnt(0)
	v_lshl_or_b32 v48, s72, 9, v0
	s_mov_b64 s[14:15], 0
	s_movk_i32 s11, 0x7fff
	s_waitcnt lgkmcnt(0)
	s_add_u32 s16, s4, 0x4078000
	s_addc_u32 s17, s5, 0
	s_mov_b32 s24, 0xffff0000
	s_mov_b64 s[18:19], 0x2000
	s_mov_b64 s[100:101], 0x8000
	s_mov_b64 s[20:21], 0x80000
	s_mov_b32 s25, 0xffff
	v_mov_b32_e32 v49, 1
	s_branch .LBB0_583

; __device__ __forceinline__ float bf_lo(unsigned w) { return __uint_as_float(w << 16); }
; __device__ __forceinline__ float bf_hi(unsigned w) { return __uint_as_float(w & 0xffff0000u); }
; __device__ __forceinline__ unsigned pk2(float lo, float hi) { return f2bf(lo) | (f2bf(hi) << 16); }
; __device__ __forceinline__ void p3_mlstm_scan(const Params& P, int tid, int vb) {
;     ...
;     for (int gid = vb * 512 + tid; gid < 8 * 8192; gid += gridDim.x * 512) {
;         const int bh = gid >> 13, idx = gid & 8191; const bool hasn = idx < 64;
;         float C0 = 0.f, C1 = 0.f, n0 = 0.f, n1 = 0.f, m = 0.f;
;         for (int j0 = 0; j0 < 256; j0 += 16) {
;             unsigned d[16]; float ml[16], gg[16]; float2 dn[16];
; #pragma unroll
;             for (int u = 0; u < 16; ++u) { const int item = bh * 256 + j0 + u; d[u] = DC[(size_t)item * 8192 + idx]; ml[u] = SC[item]; gg[u] = SC[2048 + item];
;                 dn[u] = hasn ? *(const float2*)(DN + (size_t)item * 128 + 2 * idx) : make_float2(0.f, 0.f); }
; #pragma unroll
;             for (int u = 0; u < 16; ++u) { const int item = bh * 256 + j0 + u;
;                 CS[(size_t)item * 8192 + idx] = pk2(C0, C1);
;                 if (hasn) *(float2*)(NS + (size_t)item * 128 + 2 * idx) = make_float2(n0, n1);
;                 if (idx == 0) SC[4096 + item] = m;
;                 const float mn = fmaxf(gg[u] + m, ml[u]), a = __expf(gg[u] + m - mn), bb = __expf(ml[u] - mn);
;                 C0 = a * C0 + bb * bf_lo(d[u]); C1 = a * C1 + bb * bf_hi(d[u]); n0 = a * n0 + bb * dn[u].x; n1 = a * n1 + bb * dn[u].y; m = mn; }
.LBB0_583:
	v_ashrrev_i32_e32 v3, 5, v1
	v_and_b32_e32 v6, 0xffffff00, v3
	v_and_b32_e32 v2, 0x1fff, v1
	v_ashrrev_i32_e32 v7, 31, v6
	v_and_b32_e32 v8, 0x1fff, v48
	v_cmp_gt_u32_e64 s[2:3], 64, v2
	v_cmp_eq_u32_e64 s[4:5], 0, v2
	v_lshlrev_b64 v[2:3], 2, v[6:7]
	v_lshlrev_b64 v[4:5], 9, v[6:7]
	v_lshlrev_b64 v[6:7], 15, v[6:7]
	v_lshl_or_b32 v6, v8, 2, v6
	v_mov_b32_e32 v86, 0
	v_lshl_or_b32 v4, v8, 3, v4
	v_lshl_add_u64 v[6:7], s[16:17], 0, v[6:7]
	s_mov_b32 s26, -16
	v_mov_b32_e32 v38, 0
	v_mov_b32_e32 v39, v86
	v_mov_b32_e32 v40, 0
	v_mov_b32_e32 v41, v86
	v_add_co_u32_e32 v120, vcc, 0xfbf88000, v6
	s_nop 1
	v_addc_co_u32_e32 v121, vcc, -1, v7, vcc
	global_load_dword v104, v[120:121], off
	v_lshl_add_u64 v[120:121], v[120:121], 0, s[100:101]
	global_load_dword v105, v[120:121], off
	v_lshl_add_u64 v[120:121], v[120:121], 0, s[100:101]
	global_load_dword v106, v[120:121], off
	v_lshl_add_u64 v[120:121], v[120:121], 0, s[100:101]
	global_load_dword v107, v[120:121], off
	v_lshl_add_u64 v[120:121], v[120:121], 0, s[100:101]
	global_load_dword v108, v[120:121], off
	v_lshl_add_u64 v[120:121], v[120:121], 0, s[100:101]
	global_load_dword v109, v[120:121], off
	v_lshl_add_u64 v[120:121], v[120:121], 0, s[100:101]
	global_load_dword v110, v[120:121], off
	v_lshl_add_u64 v[120:121], v[120:121], 0, s[100:101]
	global_load_dword v111, v[120:121], off
	v_lshl_add_u64 v[120:121], v[120:121], 0, s[100:101]
	global_load_dword v112, v[120:121], off
	v_lshl_add_u64 v[120:121], v[120:121], 0, s[100:101]
	global_load_dword v113, v[120:121], off
	v_lshl_add_u64 v[120:121], v[120:121], 0, s[100:101]
	global_load_dword v114, v[120:121], off
	v_lshl_add_u64 v[120:121], v[120:121], 0, s[100:101]
	global_load_dword v115, v[120:121], off
	v_lshl_add_u64 v[120:121], v[120:121], 0, s[100:101]
	global_load_dword v116, v[120:121], off
	v_lshl_add_u64 v[120:121], v[120:121], 0, s[100:101]
	global_load_dword v117, v[120:121], off
	v_lshl_add_u64 v[120:121], v[120:121], 0, s[100:101]
	global_load_dword v118, v[120:121], off
	v_lshl_add_u64 v[120:121], v[120:121], 0, s[100:101]
	global_load_dword v119, v[120:121], off
	s_waitcnt vmcnt(0)
	s_branch .LBB0_585
.LBB0_584:
	s_or_b64 exec, exec, s[22:23]
	s_waitcnt vmcnt(32)
	v_add_f32_e32 v8, v20, v53
	v_max_f32_e32 v9, v52, v52
	v_max_f32_e32 v86, v8, v9
	v_sub_f32_e32 v8, v8, v86
	v_mul_f32_e32 v9, 0x3fb8aa3b, v8
	v_sub_f32_e32 v8, v52, v86
	v_mul_f32_e32 v8, 0x3fb8aa3b, v8
	v_exp_f32_e32 v8, v8
	v_exp_f32_e32 v10, v9
	v_lshlrev_b32_e32 v18, 16, v50
	v_and_b32_e32 v19, 0xffff0000, v50
	v_pk_mul_f32 v[18:19], v[8:9], v[18:19] op_sel_hi:[0,1]
	v_pk_mul_f32 v[8:9], v[8:9], v[14:15] op_sel_hi:[0,1]
	s_add_i32 s26, s26, 16
	v_pk_fma_f32 v[40:41], v[16:17], v[10:11], v[18:19] op_sel_hi:[1,0,1]
	v_pk_fma_f32 v[38:39], v[12:13], v[10:11], v[8:9] op_sel_hi:[1,0,1]
	v_lshl_add_u64 v[2:3], v[2:3], 0, 64
	v_lshl_add_u64 v[4:5], v[4:5], 0, s[18:19]
	s_cmpk_gt_u32 s26, 0xef
	v_lshl_add_u64 v[6:7], v[6:7], 0, s[20:21]
	s_cbranch_scc1 .LBB0_582
.LBB0_585:
	s_waitcnt vmcnt(16)
	v_add_co_u32_e32 v8, vcc, 0xfbf88000, v6
	v_mov_b32_e32 v46, 0
	s_nop 0
	v_addc_co_u32_e32 v9, vcc, -1, v7, vcc
	v_mov_b32_e32 v95, v104
	v_lshl_add_u64 v[8:9], s[6:7], 0, v[2:3]
	v_add_co_u32_e32 v10, vcc, 0x1fa00000, v8
	v_mov_b32_e32 v47, 0
	s_nop 0
	v_addc_co_u32_e32 v11, vcc, 0, v9, vcc
	v_add_co_u32_e32 v12, vcc, 0x1fa02000, v8
	s_nop 1
	v_addc_co_u32_e32 v13, vcc, 0, v9, vcc
	global_load_dword v97, v[10:11], off
	global_load_dword v98, v[12:13], off
	v_lshl_add_u64 v[10:11], s[6:7], 0, v[4:5]
	s_and_saveexec_b64 s[22:23], s[2:3]
	s_cbranch_execz .LBB0_587
	v_add_co_u32_e32 v12, vcc, 0x1f800000, v10
	s_nop 1
	v_addc_co_u32_e32 v13, vcc, 0, v11, vcc
	global_load_dwordx2 v[46:47], v[12:13], off
.LBB0_587:
	s_or_b64 exec, exec, s[22:23]
	v_add_co_u32_e32 v12, vcc, 0xfbf90000, v6
	v_mov_b32_e32 v36, 0
	s_nop 0
	v_addc_co_u32_e32 v13, vcc, -1, v7, vcc
	v_mov_b32_e32 v92, v105
	v_add_co_u32_e32 v12, vcc, 0x1fa00000, v8
	v_mov_b32_e32 v44, 0
	s_nop 0
	v_addc_co_u32_e32 v13, vcc, 0, v9, vcc
	v_add_co_u32_e32 v14, vcc, 0x1fa02000, v8
	v_mov_b32_e32 v45, 0
	s_nop 0
	v_addc_co_u32_e32 v15, vcc, 0, v9, vcc
	global_load_dword v94, v[12:13], off offset:4
	global_load_dword v96, v[14:15], off offset:4
	s_and_saveexec_b64 s[22:23], s[2:3]
	s_cbranch_execz .LBB0_589
	v_add_co_u32_e32 v12, vcc, 0x1f800000, v10
	s_nop 1
	v_addc_co_u32_e32 v13, vcc, 0, v11, vcc
	global_load_dwordx2 v[44:45], v[12:13], off offset:512
.LBB0_589:
	s_or_b64 exec, exec, s[22:23]
	v_add_co_u32_e32 v12, vcc, 0xfbf98000, v6
	v_mov_b32_e32 v37, 0
	s_nop 0
	v_addc_co_u32_e32 v13, vcc, -1, v7, vcc
	v_mov_b32_e32 v89, v106
	v_add_co_u32_e32 v12, vcc, 0x1fa00000, v8
	s_nop 1
	v_addc_co_u32_e32 v13, vcc, 0, v9, vcc
	v_add_co_u32_e32 v14, vcc, 0x1fa02000, v8
	s_nop 1
	v_addc_co_u32_e32 v15, vcc, 0, v9, vcc
	global_load_dword v91, v[12:13], off offset:8
	global_load_dword v93, v[14:15], off offset:8
	s_and_saveexec_b64 s[22:23], s[2:3]
	s_cbranch_execz .LBB0_591
	v_add_co_u32_e32 v12, vcc, 0x1f800000, v10
	s_nop 1
	v_addc_co_u32_e32 v13, vcc, 0, v11, vcc
	global_load_dwordx2 v[36:37], v[12:13], off offset:1024
.LBB0_591:
	s_or_b64 exec, exec, s[22:23]
	v_add_co_u32_e32 v12, vcc, 0xfbfa0000, v6
	v_mov_b32_e32 v32, 0
	s_nop 0
	v_addc_co_u32_e32 v13, vcc, -1, v7, vcc
	v_mov_b32_e32 v85, v107
	v_add_co_u32_e32 v12, vcc, 0x1fa00000, v8
	v_mov_b32_e32 v42, 0
	s_nop 0
	v_addc_co_u32_e32 v13, vcc, 0, v9, vcc
	v_add_co_u32_e32 v14, vcc, 0x1fa02000, v8
	v_mov_b32_e32 v43, 0
	s_nop 0
	v_addc_co_u32_e32 v15, vcc, 0, v9, vcc
	global_load_dword v88, v[12:13], off offset:12
	global_load_dword v90, v[14:15], off offset:12
	s_and_saveexec_b64 s[22:23], s[2:3]
	s_cbranch_execz .LBB0_593
	v_add_co_u32_e32 v12, vcc, 0x1f800000, v10
	s_nop 1
	v_addc_co_u32_e32 v13, vcc, 0, v11, vcc
	global_load_dwordx2 v[42:43], v[12:13], off offset:1536
; __device__ __forceinline__ float bf_lo(unsigned w) { return __uint_as_float(w << 16); }
; __device__ __forceinline__ float bf_hi(unsigned w) { return __uint_as_float(w & 0xffff0000u); }
; __device__ __forceinline__ unsigned pk2(float lo, float hi) { return f2bf(lo) | (f2bf(hi) << 16); }
; __device__ __forceinline__ void p3_mlstm_scan(const Params& P, int tid, int vb) {
;     ...
;             unsigned d[16]; float ml[16], gg[16]; float2 dn[16];
; #pragma unroll
;             for (int u = 0; u < 16; ++u) { const int item = bh * 256 + j0 + u; d[u] = DC[(size_t)item * 8192 + idx]; ml[u] = SC[item]; gg[u] = SC[2048 + item];
;                 dn[u] = hasn ? *(const float2*)(DN + (size_t)item * 128 + 2 * idx) : make_float2(0.f, 0.f); }
; #pragma unroll
;             for (int u = 0; u < 16; ++u) { const int item = bh * 256 + j0 + u;
;                 CS[(size_t)item * 8192 + idx] = pk2(C0, C1);
;                 if (hasn) *(float2*)(NS + (size_t)item * 128 + 2 * idx) = make_float2(n0, n1);
;                 if (idx == 0) SC[4096 + item] = m;
;                 const float mn = fmaxf(gg[u] + m, ml[u]), a = __expf(gg[u] + m - mn), bb = __expf(ml[u] - mn);
;                 C0 = a * C0 + bb * bf_lo(d[u]); C1 = a * C1 + bb * bf_hi(d[u]); n0 = a * n0 + bb * dn[u].x; n1 = a * n1 + bb * dn[u].y; m = mn; }
.LBB0_593:
	s_or_b64 exec, exec, s[22:23]
	v_add_co_u32_e32 v12, vcc, 0xfbfa8000, v6
	v_mov_b32_e32 v33, 0
	s_nop 0
	v_addc_co_u32_e32 v13, vcc, -1, v7, vcc
	v_mov_b32_e32 v82, v108
	v_add_co_u32_e32 v12, vcc, 0x1fa00000, v8
	s_nop 1
	v_addc_co_u32_e32 v13, vcc, 0, v9, vcc
	v_add_co_u32_e32 v14, vcc, 0x1fa02000, v8
	s_nop 1
	v_addc_co_u32_e32 v15, vcc, 0, v9, vcc
	global_load_dword v84, v[12:13], off offset:16
	global_load_dword v87, v[14:15], off offset:16
	s_and_saveexec_b64 s[22:23], s[2:3]
	s_cbranch_execz .LBB0_595
	v_add_co_u32_e32 v12, vcc, 0x1f800000, v10
	s_nop 1
	v_addc_co_u32_e32 v13, vcc, 0, v11, vcc
	global_load_dwordx2 v[32:33], v[12:13], off offset:2048
.LBB0_595:
	s_or_b64 exec, exec, s[22:23]
	v_add_co_u32_e32 v12, vcc, 0xfbfb0000, v6
	v_mov_b32_e32 v28, 0
	s_nop 0
	v_addc_co_u32_e32 v13, vcc, -1, v7, vcc
	v_mov_b32_e32 v78, v109
	v_add_co_u32_e32 v12, vcc, 0x1fa00000, v8
	v_mov_b32_e32 v34, 0
	s_nop 0
	v_addc_co_u32_e32 v13, vcc, 0, v9, vcc
	v_add_co_u32_e32 v14, vcc, 0x1fa02000, v8
	v_mov_b32_e32 v35, 0
	s_nop 0
	v_addc_co_u32_e32 v15, vcc, 0, v9, vcc
	global_load_dword v81, v[12:13], off offset:20
	global_load_dword v83, v[14:15], off offset:20
	s_and_saveexec_b64 s[22:23], s[2:3]
	s_cbranch_execz .LBB0_597
	v_add_co_u32_e32 v12, vcc, 0x1f800000, v10
	s_nop 1
	v_addc_co_u32_e32 v13, vcc, 0, v11, vcc
	global_load_dwordx2 v[34:35], v[12:13], off offset:2560
.LBB0_597:
	s_or_b64 exec, exec, s[22:23]
	v_add_co_u32_e32 v12, vcc, 0xfbfb8000, v6
	v_mov_b32_e32 v29, 0
	s_nop 0
	v_addc_co_u32_e32 v13, vcc, -1, v7, vcc
	v_mov_b32_e32 v76, v110
	v_add_co_u32_e32 v12, vcc, 0x1fa00000, v8
	s_nop 1
	v_addc_co_u32_e32 v13, vcc, 0, v9, vcc
	v_add_co_u32_e32 v14, vcc, 0x1fa02000, v8
	s_nop 1
	v_addc_co_u32_e32 v15, vcc, 0, v9, vcc
	global_load_dword v79, v[12:13], off offset:24
	global_load_dword v80, v[14:15], off offset:24
	s_and_saveexec_b64 s[22:23], s[2:3]
	s_cbranch_execz .LBB0_599
	v_add_co_u32_e32 v12, vcc, 0x1f800000, v10
	s_nop 1
	v_addc_co_u32_e32 v13, vcc, 0, v11, vcc
	global_load_dwordx2 v[28:29], v[12:13], off offset:3072
.LBB0_599:
	s_or_b64 exec, exec, s[22:23]
	v_add_co_u32_e32 v12, vcc, 0xfbfc0000, v6
	v_mov_b32_e32 v24, 0
	s_nop 0
	v_addc_co_u32_e32 v13, vcc, -1, v7, vcc
	v_mov_b32_e32 v73, v111
	v_add_co_u32_e32 v12, vcc, 0x1fa00000, v8
	v_mov_b32_e32 v30, 0
	s_nop 0
	v_addc_co_u32_e32 v13, vcc, 0, v9, vcc
	v_add_co_u32_e32 v14, vcc, 0x1fa02000, v8
	v_mov_b32_e32 v31, 0
	s_nop 0
	v_addc_co_u32_e32 v15, vcc, 0, v9, vcc
	global_load_dword v75, v[12:13], off offset:28
	global_load_dword v77, v[14:15], off offset:28
	s_and_saveexec_b64 s[22:23], s[2:3]
	s_cbranch_execz .LBB0_601
	v_add_co_u32_e32 v12, vcc, 0x1f800000, v10
	s_nop 1
	v_addc_co_u32_e32 v13, vcc, 0, v11, vcc
	global_load_dwordx2 v[30:31], v[12:13], off offset:3584
.LBB0_601:
	s_or_b64 exec, exec, s[22:23]
	v_add_co_u32_e32 v12, vcc, 0xfbfc8000, v6
	v_mov_b32_e32 v25, 0
	s_nop 0
	v_addc_co_u32_e32 v13, vcc, -1, v7, vcc
	v_mov_b32_e32 v70, v112
	v_add_co_u32_e32 v12, vcc, 0x1fa00000, v8
	s_nop 1
	v_addc_co_u32_e32 v13, vcc, 0, v9, vcc
	v_add_co_u32_e32 v14, vcc, 0x1fa02000, v8
	s_nop 1
	v_addc_co_u32_e32 v15, vcc, 0, v9, vcc
	global_load_dword v72, v[12:13], off offset:32
	global_load_dword v74, v[14:15], off offset:32
	s_and_saveexec_b64 s[22:23], s[2:3]
	s_cbranch_execz .LBB0_603
	v_add_co_u32_e32 v12, vcc, 0x1f801000, v10
	s_nop 1
	v_addc_co_u32_e32 v13, vcc, 0, v11, vcc
	global_load_dwordx2 v[24:25], v[12:13], off
.LBB0_603:
	s_or_b64 exec, exec, s[22:23]
	v_add_co_u32_e32 v12, vcc, 0xfbfd0000, v6
	v_mov_b32_e32 v20, 0
	s_nop 0
	v_addc_co_u32_e32 v13, vcc, -1, v7, vcc
	v_mov_b32_e32 v67, v113
	v_add_co_u32_e32 v12, vcc, 0x1fa00000, v8
	v_mov_b32_e32 v26, 0
	s_nop 0
	v_addc_co_u32_e32 v13, vcc, 0, v9, vcc
	v_add_co_u32_e32 v14, vcc, 0x1fa02000, v8
	v_mov_b32_e32 v27, 0
	s_nop 0
	v_addc_co_u32_e32 v15, vcc, 0, v9, vcc
	global_load_dword v69, v[12:13], off offset:36
	global_load_dword v71, v[14:15], off offset:36
	s_and_saveexec_b64 s[22:23], s[2:3]
	s_cbranch_execz .LBB0_605
	v_add_co_u32_e32 v12, vcc, 0x1f801000, v10
	s_nop 1
	v_addc_co_u32_e32 v13, vcc, 0, v11, vcc
	global_load_dwordx2 v[26:27], v[12:13], off offset:512
.LBB0_605:
	s_or_b64 exec, exec, s[22:23]
	v_add_co_u32_e32 v12, vcc, 0xfbfd8000, v6
	v_mov_b32_e32 v21, 0
	s_nop 0
	v_addc_co_u32_e32 v13, vcc, -1, v7, vcc
	v_mov_b32_e32 v64, v114
	v_add_co_u32_e32 v12, vcc, 0x1fa00000, v8
	s_nop 1
	v_addc_co_u32_e32 v13, vcc, 0, v9, vcc
	v_add_co_u32_e32 v14, vcc, 0x1fa02000, v8
	s_nop 1
	v_addc_co_u32_e32 v15, vcc, 0, v9, vcc
	global_load_dword v66, v[12:13], off offset:40
	global_load_dword v68, v[14:15], off offset:40
	s_and_saveexec_b64 s[22:23], s[2:3]
	s_cbranch_execz .LBB0_607
	v_add_co_u32_e32 v12, vcc, 0x1f801000, v10
	s_nop 1
	v_addc_co_u32_e32 v13, vcc, 0, v11, vcc
	global_load_dwordx2 v[20:21], v[12:13], off offset:1024
.LBB0_607:
	s_or_b64 exec, exec, s[22:23]
	v_add_co_u32_e32 v12, vcc, 0xfbfe0000, v6
	v_mov_b32_e32 v16, 0
	s_nop 0
	v_addc_co_u32_e32 v13, vcc, -1, v7, vcc
	v_mov_b32_e32 v61, v115
	v_add_co_u32_e32 v12, vcc, 0x1fa00000, v8
	v_mov_b32_e32 v22, 0
	s_nop 0
	v_addc_co_u32_e32 v13, vcc, 0, v9, vcc
	v_add_co_u32_e32 v14, vcc, 0x1fa02000, v8
	v_mov_b32_e32 v23, 0
	s_nop 0
	v_addc_co_u32_e32 v15, vcc, 0, v9, vcc
	global_load_dword v63, v[12:13], off offset:44
	global_load_dword v65, v[14:15], off offset:44
	s_and_saveexec_b64 s[22:23], s[2:3]
	s_cbranch_execz .LBB0_609
	v_add_co_u32_e32 v12, vcc, 0x1f801000, v10
	s_nop 1
	v_addc_co_u32_e32 v13, vcc, 0, v11, vcc
	global_load_dwordx2 v[22:23], v[12:13], off offset:1536
; __device__ __forceinline__ unsigned pk2(float lo, float hi) { return f2bf(lo) | (f2bf(hi) << 16); }
; __device__ __forceinline__ void p3_mlstm_scan(const Params& P, int tid, int vb) {
;     ...
;             unsigned d[16]; float ml[16], gg[16]; float2 dn[16];
; #pragma unroll
;             for (int u = 0; u < 16; ++u) { const int item = bh * 256 + j0 + u; d[u] = DC[(size_t)item * 8192 + idx]; ml[u] = SC[item]; gg[u] = SC[2048 + item];
;                 dn[u] = hasn ? *(const float2*)(DN + (size_t)item * 128 + 2 * idx) : make_float2(0.f, 0.f); }
; #pragma unroll
;             for (int u = 0; u < 16; ++u) { const int item = bh * 256 + j0 + u;
;                 CS[(size_t)item * 8192 + idx] = pk2(C0, C1);
;                 if (hasn) *(float2*)(NS + (size_t)item * 128 + 2 * idx) = make_float2(n0, n1);
.LBB0_609:
	s_or_b64 exec, exec, s[22:23]
	v_add_co_u32_e32 v12, vcc, 0xfbfe8000, v6
	v_mov_b32_e32 v17, 0
	s_nop 0
	v_addc_co_u32_e32 v13, vcc, -1, v7, vcc
	v_mov_b32_e32 v58, v116
	v_add_co_u32_e32 v12, vcc, 0x1fa00000, v8
	s_nop 1
	v_addc_co_u32_e32 v13, vcc, 0, v9, vcc
	v_add_co_u32_e32 v14, vcc, 0x1fa02000, v8
	s_nop 1
	v_addc_co_u32_e32 v15, vcc, 0, v9, vcc
	global_load_dword v60, v[12:13], off offset:48
	global_load_dword v62, v[14:15], off offset:48
	s_and_saveexec_b64 s[22:23], s[2:3]
	s_cbranch_execz .LBB0_611
	v_add_co_u32_e32 v12, vcc, 0x1f801000, v10
	s_nop 1
	v_addc_co_u32_e32 v13, vcc, 0, v11, vcc
	global_load_dwordx2 v[16:17], v[12:13], off offset:2048
.LBB0_611:
	s_or_b64 exec, exec, s[22:23]
	v_add_co_u32_e32 v12, vcc, 0xfbff0000, v6
	v_mov_b32_e32 v18, 0
	s_nop 0
	v_addc_co_u32_e32 v13, vcc, -1, v7, vcc
	v_mov_b32_e32 v55, v117
	v_add_co_u32_e32 v12, vcc, 0x1fa00000, v8
	v_mov_b32_e32 v19, 0
	s_nop 0
	v_addc_co_u32_e32 v13, vcc, 0, v9, vcc
	v_add_co_u32_e32 v14, vcc, 0x1fa02000, v8
	s_nop 1
	v_addc_co_u32_e32 v15, vcc, 0, v9, vcc
	global_load_dword v57, v[12:13], off offset:52
	global_load_dword v59, v[14:15], off offset:52
	v_mov_b32_e32 v12, 0
	s_and_saveexec_b64 s[22:23], s[2:3]
	s_cbranch_execz .LBB0_613
	v_add_co_u32_e32 v14, vcc, 0x1f801000, v10
	s_nop 1
	v_addc_co_u32_e32 v15, vcc, 0, v11, vcc
	global_load_dwordx2 v[18:19], v[14:15], off offset:2560
.LBB0_613:
	s_or_b64 exec, exec, s[22:23]
	v_add_co_u32_e32 v14, vcc, 0xfbff8000, v6
	v_mov_b32_e32 v13, 0
	s_nop 0
	v_addc_co_u32_e32 v15, vcc, -1, v7, vcc
	v_mov_b32_e32 v51, v118
	v_add_co_u32_e32 v14, vcc, 0x1fa00000, v8
	s_nop 1
	v_addc_co_u32_e32 v15, vcc, 0, v9, vcc
	v_add_co_u32_e32 v52, vcc, 0x1fa02000, v8
	s_nop 1
	v_addc_co_u32_e32 v53, vcc, 0, v9, vcc
	global_load_dword v54, v[14:15], off offset:56
	global_load_dword v56, v[52:53], off offset:56
	s_and_saveexec_b64 s[22:23], s[2:3]
	s_cbranch_execz .LBB0_615
	v_add_co_u32_e32 v12, vcc, 0x1f801000, v10
	s_nop 1
	v_addc_co_u32_e32 v13, vcc, 0, v11, vcc
	global_load_dwordx2 v[12:13], v[12:13], off offset:3072
.LBB0_615:
	s_or_b64 exec, exec, s[22:23]
	v_add_co_u32_e32 v14, vcc, 0xfc000000, v6
	s_nop 1
	v_addc_co_u32_e32 v15, vcc, -1, v7, vcc
	v_mov_b32_e32 v50, v119
	v_add_co_u32_e32 v14, vcc, 0x1fa00000, v8
	s_nop 1
	v_addc_co_u32_e32 v15, vcc, 0, v9, vcc
	v_add_co_u32_e32 v100, vcc, 0x1fa02000, v8
	s_nop 1
	v_addc_co_u32_e32 v101, vcc, 0, v9, vcc
	global_load_dword v52, v[14:15], off offset:60
	global_load_dword v53, v[100:101], off offset:60
	v_mov_b32_e32 v14, 0
	v_mov_b32_e32 v15, 0
	s_and_saveexec_b64 s[22:23], s[2:3]
	s_cbranch_execz .LBB0_617
	v_add_co_u32_e32 v14, vcc, 0x1f801000, v10
	s_nop 1
	v_addc_co_u32_e32 v15, vcc, 0, v11, vcc
	global_load_dwordx2 v[14:15], v[14:15], off offset:3584
.LBB0_617:
	s_or_b64 exec, exec, s[22:23]
	v_add_co_u32_e32 v120, vcc, 0xfc008000, v6
	s_nop 1
	v_addc_co_u32_e32 v121, vcc, -1, v7, vcc
	global_load_dword v104, v[120:121], off
	v_lshl_add_u64 v[120:121], v[120:121], 0, s[100:101]
	global_load_dword v105, v[120:121], off
	v_lshl_add_u64 v[120:121], v[120:121], 0, s[100:101]
	global_load_dword v106, v[120:121], off
	v_lshl_add_u64 v[120:121], v[120:121], 0, s[100:101]
	global_load_dword v107, v[120:121], off
	v_lshl_add_u64 v[120:121], v[120:121], 0, s[100:101]
	global_load_dword v108, v[120:121], off
	v_lshl_add_u64 v[120:121], v[120:121], 0, s[100:101]
	global_load_dword v109, v[120:121], off
	v_lshl_add_u64 v[120:121], v[120:121], 0, s[100:101]
	global_load_dword v110, v[120:121], off
	v_lshl_add_u64 v[120:121], v[120:121], 0, s[100:101]
	global_load_dword v111, v[120:121], off
	v_lshl_add_u64 v[120:121], v[120:121], 0, s[100:101]
	global_load_dword v112, v[120:121], off
	v_lshl_add_u64 v[120:121], v[120:121], 0, s[100:101]
	global_load_dword v113, v[120:121], off
	v_lshl_add_u64 v[120:121], v[120:121], 0, s[100:101]
	global_load_dword v114, v[120:121], off
	v_lshl_add_u64 v[120:121], v[120:121], 0, s[100:101]
	global_load_dword v115, v[120:121], off
	v_lshl_add_u64 v[120:121], v[120:121], 0, s[100:101]
	global_load_dword v116, v[120:121], off
	v_lshl_add_u64 v[120:121], v[120:121], 0, s[100:101]
	global_load_dword v117, v[120:121], off
	v_lshl_add_u64 v[120:121], v[120:121], 0, s[100:101]
	global_load_dword v118, v[120:121], off
	v_lshl_add_u64 v[120:121], v[120:121], 0, s[100:101]
	global_load_dword v119, v[120:121], off
	v_bfe_u32 v99, v40, 16, 1
	v_add3_u32 v99, v40, v99, s11
	v_bfe_u32 v100, v41, 16, 1
	v_lshrrev_b32_e32 v99, 16, v99
	v_add3_u32 v100, v41, v100, s11
	v_and_or_b32 v99, v100, s24, v99
	v_add_co_u32_e32 v100, vcc, 0xfff88000, v6
	s_nop 1
	v_addc_co_u32_e32 v101, vcc, -1, v7, vcc
	global_store_dword v[100:101], v99, off
	s_and_saveexec_b64 s[22:23], s[2:3]
	s_cbranch_execz .LBB0_619
	v_add_co_u32_e32 v100, vcc, 0x1f900000, v10
	s_nop 1
	v_addc_co_u32_e32 v101, vcc, 0, v11, vcc
	global_store_dwordx2 v[100:101], v[38:39], off

; __device__ __forceinline__ float bf_lo(unsigned w) { return __uint_as_float(w << 16); }
; __device__ __forceinline__ float bf_hi(unsigned w) { return __uint_as_float(w & 0xffff0000u); }
; __device__ __forceinline__ unsigned pk2(float lo, float hi) { return f2bf(lo) | (f2bf(hi) << 16); }
; __device__ __forceinline__ void p3_mlstm_scan(const Params& P, int tid, int vb) {
;     ...
;             for (int u = 0; u < 16; ++u) { const int item = bh * 256 + j0 + u;
;                 CS[(size_t)item * 8192 + idx] = pk2(C0, C1);
;                 if (hasn) *(float2*)(NS + (size_t)item * 128 + 2 * idx) = make_float2(n0, n1);
;                 if (idx == 0) SC[4096 + item] = m;
;                 const float mn = fmaxf(gg[u] + m, ml[u]), a = __expf(gg[u] + m - mn), bb = __expf(ml[u] - mn);
;                 C0 = a * C0 + bb * bf_lo(d[u]); C1 = a * C1 + bb * bf_hi(d[u]); n0 = a * n0 + bb * dn[u].x; n1 = a * n1 + bb * dn[u].y; m = mn; }
.LBB0_621:
	s_or_b64 exec, exec, s[22:23]
	s_waitcnt vmcnt(47)
	v_add_f32_e32 v98, v86, v98
	v_max_f32_e32 v86, v97, v97
	v_max_f32_e32 v86, v98, v86
	v_sub_f32_e32 v97, v97, v86
	v_sub_f32_e32 v98, v98, v86
	v_mul_f32_e32 v97, 0x3fb8aa3b, v97
	v_mul_f32_e32 v99, 0x3fb8aa3b, v98
	v_exp_f32_e32 v98, v97
	v_exp_f32_e32 v100, v99
	v_lshlrev_b32_e32 v102, 16, v95
	v_and_b32_e32 v103, 0xffff0000, v95
	v_pk_mul_f32 v[102:103], v[98:99], v[102:103] op_sel_hi:[0,1]
	v_pk_fma_f32 v[40:41], v[40:41], v[100:101], v[102:103] op_sel_hi:[1,0,1]
	v_pk_mul_f32 v[46:47], v[98:99], v[46:47] op_sel_hi:[0,1]
	v_pk_fma_f32 v[38:39], v[38:39], v[100:101], v[46:47] op_sel_hi:[1,0,1]
	v_bfe_u32 v46, v40, 16, 1
	v_add3_u32 v46, v40, v46, s11
	v_bfe_u32 v47, v41, 16, 1
	v_lshrrev_b32_e32 v46, 16, v46
	v_add3_u32 v47, v41, v47, s11
	v_and_or_b32 v95, v47, s24, v46
	v_add_co_u32_e32 v46, vcc, 0xfff90000, v6
	s_nop 1
	v_addc_co_u32_e32 v47, vcc, -1, v7, vcc
	global_store_dword v[46:47], v95, off
	s_and_saveexec_b64 s[22:23], s[2:3]
	s_cbranch_execz .LBB0_623
	v_add_co_u32_e32 v46, vcc, 0x1f900000, v10
	s_nop 1
	v_addc_co_u32_e32 v47, vcc, 0, v11, vcc
	global_store_dwordx2 v[46:47], v[38:39], off offset:512

; __device__ __forceinline__ float bf_lo(unsigned w) { return __uint_as_float(w << 16); }
; __device__ __forceinline__ float bf_hi(unsigned w) { return __uint_as_float(w & 0xffff0000u); }
; __device__ __forceinline__ unsigned pk2(float lo, float hi) { return f2bf(lo) | (f2bf(hi) << 16); }
; __device__ __forceinline__ void p3_mlstm_scan(const Params& P, int tid, int vb) {
;     ...
;             for (int u = 0; u < 16; ++u) { const int item = bh * 256 + j0 + u;
;                 CS[(size_t)item * 8192 + idx] = pk2(C0, C1);
;                 if (hasn) *(float2*)(NS + (size_t)item * 128 + 2 * idx) = make_float2(n0, n1);
;                 if (idx == 0) SC[4096 + item] = m;
;                 const float mn = fmaxf(gg[u] + m, ml[u]), a = __expf(gg[u] + m - mn), bb = __expf(ml[u] - mn);
;                 C0 = a * C0 + bb * bf_lo(d[u]); C1 = a * C1 + bb * bf_hi(d[u]); n0 = a * n0 + bb * dn[u].x; n1 = a * n1 + bb * dn[u].y; m = mn; }
.LBB0_625:
	s_or_b64 exec, exec, s[22:23]
	s_waitcnt vmcnt(46)
	v_add_f32_e32 v47, v86, v96
	v_max_f32_e32 v46, v94, v94
	v_max_f32_e32 v46, v47, v46
	v_sub_f32_e32 v86, v94, v46
	v_sub_f32_e32 v47, v47, v46
	v_mul_f32_e32 v86, 0x3fb8aa3b, v86
	v_mul_f32_e32 v47, 0x3fb8aa3b, v47
	v_exp_f32_e32 v86, v86
	v_exp_f32_e32 v94, v47
	v_lshlrev_b32_e32 v96, 16, v92
	v_and_b32_e32 v97, 0xffff0000, v92
	s_waitcnt vmcnt(40)
	v_pk_mul_f32 v[96:97], v[86:87], v[96:97] op_sel_hi:[0,1]
	v_pk_fma_f32 v[40:41], v[40:41], v[94:95], v[96:97] op_sel_hi:[1,0,1]
	v_pk_mul_f32 v[44:45], v[86:87], v[44:45] op_sel_hi:[0,1]
	v_pk_fma_f32 v[38:39], v[38:39], v[94:95], v[44:45] op_sel_hi:[1,0,1]
	v_bfe_u32 v44, v40, 16, 1
	v_add3_u32 v44, v40, v44, s11
	v_bfe_u32 v45, v41, 16, 1
	v_lshrrev_b32_e32 v44, 16, v44
	v_add3_u32 v45, v41, v45, s11
	v_and_or_b32 v47, v45, s24, v44
	v_add_co_u32_e32 v44, vcc, 0xfff98000, v6
	s_nop 1
	v_addc_co_u32_e32 v45, vcc, -1, v7, vcc
	global_store_dword v[44:45], v47, off
	s_and_saveexec_b64 s[22:23], s[2:3]
	s_cbranch_execz .LBB0_627
	v_add_co_u32_e32 v44, vcc, 0x1f900000, v10
	s_nop 1
	v_addc_co_u32_e32 v45, vcc, 0, v11, vcc
	global_store_dwordx2 v[44:45], v[38:39], off offset:1024

; __device__ __forceinline__ float bf_lo(unsigned w) { return __uint_as_float(w << 16); }
; __device__ __forceinline__ float bf_hi(unsigned w) { return __uint_as_float(w & 0xffff0000u); }
; __device__ __forceinline__ unsigned pk2(float lo, float hi) { return f2bf(lo) | (f2bf(hi) << 16); }
; __device__ __forceinline__ void p3_mlstm_scan(const Params& P, int tid, int vb) {
;     ...
;             for (int u = 0; u < 16; ++u) { const int item = bh * 256 + j0 + u;
;                 CS[(size_t)item * 8192 + idx] = pk2(C0, C1);
;                 if (hasn) *(float2*)(NS + (size_t)item * 128 + 2 * idx) = make_float2(n0, n1);
;                 if (idx == 0) SC[4096 + item] = m;
;                 const float mn = fmaxf(gg[u] + m, ml[u]), a = __expf(gg[u] + m - mn), bb = __expf(ml[u] - mn);
;                 C0 = a * C0 + bb * bf_lo(d[u]); C1 = a * C1 + bb * bf_hi(d[u]); n0 = a * n0 + bb * dn[u].x; n1 = a * n1 + bb * dn[u].y; m = mn; }
.LBB0_641:
	s_or_b64 exec, exec, s[22:23]
	s_waitcnt vmcnt(42)
	v_add_f32_e32 v36, v40, v83
	v_max_f32_e32 v37, v81, v81
	v_max_f32_e32 v40, v36, v37
	v_sub_f32_e32 v37, v81, v40
	v_sub_f32_e32 v36, v36, v40
	v_mul_f32_e32 v37, 0x3fb8aa3b, v37
	v_mul_f32_e32 v36, 0x3fb8aa3b, v36
	v_exp_f32_e32 v42, v37
	v_exp_f32_e32 v44, v36
	v_lshlrev_b32_e32 v36, 16, v78
	v_and_b32_e32 v37, 0xffff0000, v78
	v_pk_mul_f32 v[36:37], v[42:43], v[36:37] op_sel_hi:[0,1]
	v_pk_fma_f32 v[36:37], v[38:39], v[44:45], v[36:37] op_sel_hi:[1,0,1]
	v_pk_mul_f32 v[34:35], v[42:43], v[34:35] op_sel_hi:[0,1]
	v_pk_fma_f32 v[32:33], v[32:33], v[44:45], v[34:35] op_sel_hi:[1,0,1]
	v_bfe_u32 v34, v36, 16, 1
	v_add3_u32 v34, v36, v34, s11
	v_bfe_u32 v35, v37, 16, 1
	v_lshrrev_b32_e32 v34, 16, v34
	v_add3_u32 v35, v37, v35, s11
	v_and_or_b32 v38, v35, s24, v34
	v_add_co_u32_e32 v34, vcc, 0xfffb8000, v6
	s_nop 1
	v_addc_co_u32_e32 v35, vcc, -1, v7, vcc
	global_store_dword v[34:35], v38, off
	s_and_saveexec_b64 s[22:23], s[2:3]
	s_cbranch_execz .LBB0_643
	v_add_co_u32_e32 v34, vcc, 0x1f900000, v10
	s_nop 1
	v_addc_co_u32_e32 v35, vcc, 0, v11, vcc
	global_store_dwordx2 v[34:35], v[32:33], off offset:3072

; __device__ __forceinline__ float bf_lo(unsigned w) { return __uint_as_float(w << 16); }
; __device__ __forceinline__ float bf_hi(unsigned w) { return __uint_as_float(w & 0xffff0000u); }
; __device__ __forceinline__ unsigned pk2(float lo, float hi) { return f2bf(lo) | (f2bf(hi) << 16); }
; __device__ __forceinline__ void p3_mlstm_scan(const Params& P, int tid, int vb) {
;     ...
;             for (int u = 0; u < 16; ++u) { const int item = bh * 256 + j0 + u;
;                 CS[(size_t)item * 8192 + idx] = pk2(C0, C1);
;                 if (hasn) *(float2*)(NS + (size_t)item * 128 + 2 * idx) = make_float2(n0, n1);
;                 if (idx == 0) SC[4096 + item] = m;
;                 const float mn = fmaxf(gg[u] + m, ml[u]), a = __expf(gg[u] + m - mn), bb = __expf(ml[u] - mn);
;                 C0 = a * C0 + bb * bf_lo(d[u]); C1 = a * C1 + bb * bf_hi(d[u]); n0 = a * n0 + bb * dn[u].x; n1 = a * n1 + bb * dn[u].y; m = mn; }
.LBB0_645:
	s_or_b64 exec, exec, s[22:23]
	s_waitcnt vmcnt(41)
	v_add_f32_e32 v34, v40, v80
	v_max_f32_e32 v35, v79, v79
	v_max_f32_e32 v38, v34, v35
	v_sub_f32_e32 v35, v79, v38
	v_sub_f32_e32 v34, v34, v38
	v_mul_f32_e32 v35, 0x3fb8aa3b, v35
	v_mul_f32_e32 v34, 0x3fb8aa3b, v34
	v_exp_f32_e32 v40, v35
	v_exp_f32_e32 v42, v34
	v_lshlrev_b32_e32 v34, 16, v76
	v_and_b32_e32 v35, 0xffff0000, v76
	v_pk_mul_f32 v[34:35], v[40:41], v[34:35] op_sel_hi:[0,1]
	v_pk_fma_f32 v[34:35], v[36:37], v[42:43], v[34:35] op_sel_hi:[1,0,1]
	v_pk_mul_f32 v[28:29], v[40:41], v[28:29] op_sel_hi:[0,1]
	v_pk_fma_f32 v[28:29], v[32:33], v[42:43], v[28:29] op_sel_hi:[1,0,1]
	v_bfe_u32 v32, v34, 16, 1
	v_add3_u32 v32, v34, v32, s11
	v_bfe_u32 v33, v35, 16, 1
	v_lshrrev_b32_e32 v32, 16, v32
	v_add3_u32 v33, v35, v33, s11
	v_and_or_b32 v36, v33, s24, v32
	v_add_co_u32_e32 v32, vcc, 0xfffc0000, v6
	s_nop 1
	v_addc_co_u32_e32 v33, vcc, -1, v7, vcc
	global_store_dword v[32:33], v36, off
	s_and_saveexec_b64 s[22:23], s[2:3]
	s_cbranch_execz .LBB0_647
	v_add_co_u32_e32 v32, vcc, 0x1f900000, v10
	s_nop 1
	v_addc_co_u32_e32 v33, vcc, 0, v11, vcc
	global_store_dwordx2 v[32:33], v[28:29], off offset:3584

; __device__ __forceinline__ float bf_lo(unsigned w) { return __uint_as_float(w << 16); }
; __device__ __forceinline__ float bf_hi(unsigned w) { return __uint_as_float(w & 0xffff0000u); }
; __device__ __forceinline__ unsigned pk2(float lo, float hi) { return f2bf(lo) | (f2bf(hi) << 16); }
; __device__ __forceinline__ void p3_mlstm_scan(const Params& P, int tid, int vb) {
;     ...
;             for (int u = 0; u < 16; ++u) { const int item = bh * 256 + j0 + u;
;                 CS[(size_t)item * 8192 + idx] = pk2(C0, C1);
;                 if (hasn) *(float2*)(NS + (size_t)item * 128 + 2 * idx) = make_float2(n0, n1);
;                 if (idx == 0) SC[4096 + item] = m;
;                 const float mn = fmaxf(gg[u] + m, ml[u]), a = __expf(gg[u] + m - mn), bb = __expf(ml[u] - mn);
;                 C0 = a * C0 + bb * bf_lo(d[u]); C1 = a * C1 + bb * bf_hi(d[u]); n0 = a * n0 + bb * dn[u].x; n1 = a * n1 + bb * dn[u].y; m = mn; }
.LBB0_649:
	s_or_b64 exec, exec, s[22:23]
	s_waitcnt vmcnt(40)
	v_add_f32_e32 v32, v38, v77
	v_max_f32_e32 v33, v75, v75
	v_max_f32_e32 v36, v32, v33
	v_sub_f32_e32 v33, v75, v36
	v_sub_f32_e32 v32, v32, v36
	v_mul_f32_e32 v33, 0x3fb8aa3b, v33
	v_mul_f32_e32 v32, 0x3fb8aa3b, v32
	v_exp_f32_e32 v38, v33
	v_exp_f32_e32 v40, v32
	v_lshlrev_b32_e32 v32, 16, v73
	v_and_b32_e32 v33, 0xffff0000, v73
	v_pk_mul_f32 v[32:33], v[38:39], v[32:33] op_sel_hi:[0,1]
	v_pk_fma_f32 v[32:33], v[34:35], v[40:41], v[32:33] op_sel_hi:[1,0,1]
	v_pk_mul_f32 v[30:31], v[38:39], v[30:31] op_sel_hi:[0,1]
	v_pk_fma_f32 v[28:29], v[28:29], v[40:41], v[30:31] op_sel_hi:[1,0,1]
	v_bfe_u32 v30, v32, 16, 1
	v_add3_u32 v30, v32, v30, s11
	v_bfe_u32 v31, v33, 16, 1
	v_lshrrev_b32_e32 v30, 16, v30
	v_add3_u32 v31, v33, v31, s11
	v_and_or_b32 v34, v31, s24, v30
	v_add_co_u32_e32 v30, vcc, 0xfffc8000, v6
	s_nop 1
	v_addc_co_u32_e32 v31, vcc, -1, v7, vcc
	global_store_dword v[30:31], v34, off
	s_and_saveexec_b64 s[22:23], s[2:3]
	s_cbranch_execz .LBB0_651
	v_add_co_u32_e32 v30, vcc, 0x1f901000, v10
	s_nop 1
	v_addc_co_u32_e32 v31, vcc, 0, v11, vcc
	global_store_dwordx2 v[30:31], v[28:29], off

; __device__ __forceinline__ float bf_lo(unsigned w) { return __uint_as_float(w << 16); }
; __device__ __forceinline__ float bf_hi(unsigned w) { return __uint_as_float(w & 0xffff0000u); }
; __device__ __forceinline__ unsigned pk2(float lo, float hi) { return f2bf(lo) | (f2bf(hi) << 16); }
; __device__ __forceinline__ void p3_mlstm_scan(const Params& P, int tid, int vb) {
;     ...
;             for (int u = 0; u < 16; ++u) { const int item = bh * 256 + j0 + u;
;                 CS[(size_t)item * 8192 + idx] = pk2(C0, C1);
;                 if (hasn) *(float2*)(NS + (size_t)item * 128 + 2 * idx) = make_float2(n0, n1);
;                 if (idx == 0) SC[4096 + item] = m;
;                 const float mn = fmaxf(gg[u] + m, ml[u]), a = __expf(gg[u] + m - mn), bb = __expf(ml[u] - mn);
;                 C0 = a * C0 + bb * bf_lo(d[u]); C1 = a * C1 + bb * bf_hi(d[u]); n0 = a * n0 + bb * dn[u].x; n1 = a * n1 + bb * dn[u].y; m = mn; }
.LBB0_653:
	s_or_b64 exec, exec, s[22:23]
	s_waitcnt vmcnt(39)
	v_add_f32_e32 v30, v36, v74
	v_max_f32_e32 v31, v72, v72
	v_max_f32_e32 v34, v30, v31
	v_sub_f32_e32 v31, v72, v34
	v_sub_f32_e32 v30, v30, v34
	v_mul_f32_e32 v31, 0x3fb8aa3b, v31
	v_mul_f32_e32 v30, 0x3fb8aa3b, v30
	v_exp_f32_e32 v36, v31
	v_exp_f32_e32 v38, v30
	v_lshlrev_b32_e32 v30, 16, v70
	v_and_b32_e32 v31, 0xffff0000, v70
	v_pk_mul_f32 v[30:31], v[36:37], v[30:31] op_sel_hi:[0,1]
	v_pk_fma_f32 v[30:31], v[32:33], v[38:39], v[30:31] op_sel_hi:[1,0,1]
	v_pk_mul_f32 v[24:25], v[36:37], v[24:25] op_sel_hi:[0,1]
	v_pk_fma_f32 v[24:25], v[28:29], v[38:39], v[24:25] op_sel_hi:[1,0,1]
	v_bfe_u32 v28, v30, 16, 1
	v_add3_u32 v28, v30, v28, s11
	v_bfe_u32 v29, v31, 16, 1
	v_lshrrev_b32_e32 v28, 16, v28
	v_add3_u32 v29, v31, v29, s11
	v_and_or_b32 v32, v29, s24, v28
	v_add_co_u32_e32 v28, vcc, 0xfffd0000, v6
	s_nop 1
	v_addc_co_u32_e32 v29, vcc, -1, v7, vcc
	global_store_dword v[28:29], v32, off
	s_and_saveexec_b64 s[22:23], s[2:3]
	s_cbranch_execz .LBB0_655
	v_add_co_u32_e32 v28, vcc, 0x1f901000, v10
	s_nop 1
	v_addc_co_u32_e32 v29, vcc, 0, v11, vcc
	global_store_dwordx2 v[28:29], v[24:25], off offset:512

; __device__ __forceinline__ float bf_lo(unsigned w) { return __uint_as_float(w << 16); }
; __device__ __forceinline__ float bf_hi(unsigned w) { return __uint_as_float(w & 0xffff0000u); }
; __device__ __forceinline__ unsigned pk2(float lo, float hi) { return f2bf(lo) | (f2bf(hi) << 16); }
; __device__ __forceinline__ void p3_mlstm_scan(const Params& P, int tid, int vb) {
;     ...
;             for (int u = 0; u < 16; ++u) { const int item = bh * 256 + j0 + u;
;                 CS[(size_t)item * 8192 + idx] = pk2(C0, C1);
;                 if (hasn) *(float2*)(NS + (size_t)item * 128 + 2 * idx) = make_float2(n0, n1);
;                 if (idx == 0) SC[4096 + item] = m;
;                 const float mn = fmaxf(gg[u] + m, ml[u]), a = __expf(gg[u] + m - mn), bb = __expf(ml[u] - mn);
;                 C0 = a * C0 + bb * bf_lo(d[u]); C1 = a * C1 + bb * bf_hi(d[u]); n0 = a * n0 + bb * dn[u].x; n1 = a * n1 + bb * dn[u].y; m = mn; }
.LBB0_657:
	s_or_b64 exec, exec, s[22:23]
	s_waitcnt vmcnt(38)
	v_add_f32_e32 v28, v34, v71
	v_max_f32_e32 v29, v69, v69
	v_max_f32_e32 v32, v28, v29
	v_sub_f32_e32 v29, v69, v32
	v_sub_f32_e32 v28, v28, v32
	v_mul_f32_e32 v29, 0x3fb8aa3b, v29
	v_mul_f32_e32 v28, 0x3fb8aa3b, v28
	v_exp_f32_e32 v34, v29
	v_exp_f32_e32 v36, v28
	v_lshlrev_b32_e32 v28, 16, v67
	v_and_b32_e32 v29, 0xffff0000, v67
	v_pk_mul_f32 v[28:29], v[34:35], v[28:29] op_sel_hi:[0,1]
	v_pk_fma_f32 v[28:29], v[30:31], v[36:37], v[28:29] op_sel_hi:[1,0,1]
	v_pk_mul_f32 v[26:27], v[34:35], v[26:27] op_sel_hi:[0,1]
	v_pk_fma_f32 v[24:25], v[24:25], v[36:37], v[26:27] op_sel_hi:[1,0,1]
	v_bfe_u32 v26, v28, 16, 1
	v_add3_u32 v26, v28, v26, s11
	v_bfe_u32 v27, v29, 16, 1
	v_lshrrev_b32_e32 v26, 16, v26
	v_add3_u32 v27, v29, v27, s11
	v_and_or_b32 v30, v27, s24, v26
	v_add_co_u32_e32 v26, vcc, 0xfffd8000, v6
	s_nop 1
	v_addc_co_u32_e32 v27, vcc, -1, v7, vcc
	global_store_dword v[26:27], v30, off
	s_and_saveexec_b64 s[22:23], s[2:3]
	s_cbranch_execz .LBB0_659
	v_add_co_u32_e32 v26, vcc, 0x1f901000, v10
	s_nop 1
	v_addc_co_u32_e32 v27, vcc, 0, v11, vcc
	global_store_dwordx2 v[26:27], v[24:25], off offset:1024

; __device__ __forceinline__ float bf_lo(unsigned w) { return __uint_as_float(w << 16); }
; __device__ __forceinline__ float bf_hi(unsigned w) { return __uint_as_float(w & 0xffff0000u); }
; __device__ __forceinline__ unsigned pk2(float lo, float hi) { return f2bf(lo) | (f2bf(hi) << 16); }
; __device__ __forceinline__ void p3_mlstm_scan(const Params& P, int tid, int vb) {
;     ...
;             for (int u = 0; u < 16; ++u) { const int item = bh * 256 + j0 + u;
;                 CS[(size_t)item * 8192 + idx] = pk2(C0, C1);
;                 if (hasn) *(float2*)(NS + (size_t)item * 128 + 2 * idx) = make_float2(n0, n1);
;                 if (idx == 0) SC[4096 + item] = m;
;                 const float mn = fmaxf(gg[u] + m, ml[u]), a = __expf(gg[u] + m - mn), bb = __expf(ml[u] - mn);
;                 C0 = a * C0 + bb * bf_lo(d[u]); C1 = a * C1 + bb * bf_hi(d[u]); n0 = a * n0 + bb * dn[u].x; n1 = a * n1 + bb * dn[u].y; m = mn; }
.LBB0_661:
	s_or_b64 exec, exec, s[22:23]
	s_waitcnt vmcnt(37)
	v_add_f32_e32 v26, v32, v68
	v_max_f32_e32 v27, v66, v66
	v_max_f32_e32 v30, v26, v27
	v_sub_f32_e32 v27, v66, v30
	v_sub_f32_e32 v26, v26, v30
	v_mul_f32_e32 v27, 0x3fb8aa3b, v27
	v_mul_f32_e32 v26, 0x3fb8aa3b, v26
	v_exp_f32_e32 v32, v27
	v_exp_f32_e32 v34, v26
	v_lshlrev_b32_e32 v26, 16, v64
	v_and_b32_e32 v27, 0xffff0000, v64
	v_pk_mul_f32 v[26:27], v[32:33], v[26:27] op_sel_hi:[0,1]
	v_pk_fma_f32 v[26:27], v[28:29], v[34:35], v[26:27] op_sel_hi:[1,0,1]
	v_pk_mul_f32 v[20:21], v[32:33], v[20:21] op_sel_hi:[0,1]
	v_pk_fma_f32 v[20:21], v[24:25], v[34:35], v[20:21] op_sel_hi:[1,0,1]
	v_bfe_u32 v24, v26, 16, 1
	v_add3_u32 v24, v26, v24, s11
	v_bfe_u32 v25, v27, 16, 1
	v_lshrrev_b32_e32 v24, 16, v24
	v_add3_u32 v25, v27, v25, s11
	v_and_or_b32 v28, v25, s24, v24
	v_add_co_u32_e32 v24, vcc, 0xfffe0000, v6
	s_nop 1
	v_addc_co_u32_e32 v25, vcc, -1, v7, vcc
	global_store_dword v[24:25], v28, off
	s_and_saveexec_b64 s[22:23], s[2:3]
	s_cbranch_execz .LBB0_663
	v_add_co_u32_e32 v24, vcc, 0x1f901000, v10
	s_nop 1
	v_addc_co_u32_e32 v25, vcc, 0, v11, vcc
	global_store_dwordx2 v[24:25], v[20:21], off offset:1536

; __device__ __forceinline__ float bf_lo(unsigned w) { return __uint_as_float(w << 16); }
; __device__ __forceinline__ float bf_hi(unsigned w) { return __uint_as_float(w & 0xffff0000u); }
; __device__ __forceinline__ unsigned pk2(float lo, float hi) { return f2bf(lo) | (f2bf(hi) << 16); }
; __device__ __forceinline__ void p3_mlstm_scan(const Params& P, int tid, int vb) {
;     ...
;             for (int u = 0; u < 16; ++u) { const int item = bh * 256 + j0 + u;
;                 CS[(size_t)item * 8192 + idx] = pk2(C0, C1);
;                 if (hasn) *(float2*)(NS + (size_t)item * 128 + 2 * idx) = make_float2(n0, n1);
;                 if (idx == 0) SC[4096 + item] = m;
;                 const float mn = fmaxf(gg[u] + m, ml[u]), a = __expf(gg[u] + m - mn), bb = __expf(ml[u] - mn);
;                 C0 = a * C0 + bb * bf_lo(d[u]); C1 = a * C1 + bb * bf_hi(d[u]); n0 = a * n0 + bb * dn[u].x; n1 = a * n1 + bb * dn[u].y; m = mn; }
.LBB0_665:
	s_or_b64 exec, exec, s[22:23]
	s_waitcnt vmcnt(36)
	v_add_f32_e32 v24, v30, v65
	v_max_f32_e32 v25, v63, v63
	v_max_f32_e32 v28, v24, v25
	v_sub_f32_e32 v25, v63, v28
	v_sub_f32_e32 v24, v24, v28
	v_mul_f32_e32 v25, 0x3fb8aa3b, v25
	v_mul_f32_e32 v24, 0x3fb8aa3b, v24
	v_exp_f32_e32 v30, v25
	v_exp_f32_e32 v32, v24
	v_lshlrev_b32_e32 v24, 16, v61
	v_and_b32_e32 v25, 0xffff0000, v61
	v_pk_mul_f32 v[24:25], v[30:31], v[24:25] op_sel_hi:[0,1]
	v_pk_fma_f32 v[24:25], v[26:27], v[32:33], v[24:25] op_sel_hi:[1,0,1]
	v_pk_mul_f32 v[22:23], v[30:31], v[22:23] op_sel_hi:[0,1]
	v_pk_fma_f32 v[20:21], v[20:21], v[32:33], v[22:23] op_sel_hi:[1,0,1]
	v_bfe_u32 v22, v24, 16, 1
	v_add3_u32 v22, v24, v22, s11
	v_bfe_u32 v23, v25, 16, 1
	v_lshrrev_b32_e32 v22, 16, v22
	v_add3_u32 v23, v25, v23, s11
	v_and_or_b32 v26, v23, s24, v22
	v_add_co_u32_e32 v22, vcc, 0xfffe8000, v6
	s_nop 1
	v_addc_co_u32_e32 v23, vcc, -1, v7, vcc
	global_store_dword v[22:23], v26, off
	s_and_saveexec_b64 s[22:23], s[2:3]
	s_cbranch_execz .LBB0_667
	v_add_co_u32_e32 v22, vcc, 0x1f901000, v10
	s_nop 1
	v_addc_co_u32_e32 v23, vcc, 0, v11, vcc
	global_store_dwordx2 v[22:23], v[20:21], off offset:2048

; __device__ __forceinline__ float bf_lo(unsigned w) { return __uint_as_float(w << 16); }
; __device__ __forceinline__ float bf_hi(unsigned w) { return __uint_as_float(w & 0xffff0000u); }
; __device__ __forceinline__ unsigned pk2(float lo, float hi) { return f2bf(lo) | (f2bf(hi) << 16); }
; __device__ __forceinline__ void p3_mlstm_scan(const Params& P, int tid, int vb) {
;     ...
;             for (int u = 0; u < 16; ++u) { const int item = bh * 256 + j0 + u;
;                 CS[(size_t)item * 8192 + idx] = pk2(C0, C1);
;                 if (hasn) *(float2*)(NS + (size_t)item * 128 + 2 * idx) = make_float2(n0, n1);
;                 if (idx == 0) SC[4096 + item] = m;
;                 const float mn = fmaxf(gg[u] + m, ml[u]), a = __expf(gg[u] + m - mn), bb = __expf(ml[u] - mn);
;                 C0 = a * C0 + bb * bf_lo(d[u]); C1 = a * C1 + bb * bf_hi(d[u]); n0 = a * n0 + bb * dn[u].x; n1 = a * n1 + bb * dn[u].y; m = mn; }
.LBB0_669:
	s_or_b64 exec, exec, s[22:23]
	s_waitcnt vmcnt(35)
	v_add_f32_e32 v22, v28, v62
	v_max_f32_e32 v23, v60, v60
	v_max_f32_e32 v26, v22, v23
	v_sub_f32_e32 v23, v60, v26
	v_sub_f32_e32 v22, v22, v26
	v_mul_f32_e32 v23, 0x3fb8aa3b, v23
	v_mul_f32_e32 v22, 0x3fb8aa3b, v22
	v_exp_f32_e32 v28, v23
	v_exp_f32_e32 v30, v22
	v_lshlrev_b32_e32 v22, 16, v58
	v_and_b32_e32 v23, 0xffff0000, v58
	v_pk_mul_f32 v[22:23], v[28:29], v[22:23] op_sel_hi:[0,1]
	v_pk_fma_f32 v[22:23], v[24:25], v[30:31], v[22:23] op_sel_hi:[1,0,1]
	v_pk_mul_f32 v[16:17], v[28:29], v[16:17] op_sel_hi:[0,1]
	v_pk_fma_f32 v[20:21], v[20:21], v[30:31], v[16:17] op_sel_hi:[1,0,1]
	v_bfe_u32 v16, v22, 16, 1
	v_add3_u32 v16, v22, v16, s11
	v_bfe_u32 v17, v23, 16, 1
	v_lshrrev_b32_e32 v16, 16, v16
	v_add3_u32 v17, v23, v17, s11
	v_and_or_b32 v24, v17, s24, v16
	v_add_co_u32_e32 v16, vcc, 0xffff0000, v6
	s_nop 1
	v_addc_co_u32_e32 v17, vcc, -1, v7, vcc
	global_store_dword v[16:17], v24, off
	s_and_saveexec_b64 s[22:23], s[2:3]
	s_cbranch_execz .LBB0_671
	v_add_co_u32_e32 v16, vcc, 0x1f901000, v10
	s_nop 1
	v_addc_co_u32_e32 v17, vcc, 0, v11, vcc
	global_store_dwordx2 v[16:17], v[20:21], off offset:2560

; __device__ __forceinline__ float bf_lo(unsigned w) { return __uint_as_float(w << 16); }
; __device__ __forceinline__ float bf_hi(unsigned w) { return __uint_as_float(w & 0xffff0000u); }
; __device__ __forceinline__ unsigned pk2(float lo, float hi) { return f2bf(lo) | (f2bf(hi) << 16); }
; __device__ __forceinline__ void p3_mlstm_scan(const Params& P, int tid, int vb) {
;     ...
;             for (int u = 0; u < 16; ++u) { const int item = bh * 256 + j0 + u;
;                 CS[(size_t)item * 8192 + idx] = pk2(C0, C1);
;                 if (hasn) *(float2*)(NS + (size_t)item * 128 + 2 * idx) = make_float2(n0, n1);
;                 if (idx == 0) SC[4096 + item] = m;
;                 const float mn = fmaxf(gg[u] + m, ml[u]), a = __expf(gg[u] + m - mn), bb = __expf(ml[u] - mn);
;                 C0 = a * C0 + bb * bf_lo(d[u]); C1 = a * C1 + bb * bf_hi(d[u]); n0 = a * n0 + bb * dn[u].x; n1 = a * n1 + bb * dn[u].y; m = mn; }
.LBB0_673:
	s_or_b64 exec, exec, s[22:23]
	s_waitcnt vmcnt(34)
	v_add_f32_e32 v16, v26, v59
	v_max_f32_e32 v17, v57, v57
	v_max_f32_e32 v24, v16, v17
	v_sub_f32_e32 v17, v57, v24
	v_sub_f32_e32 v16, v16, v24
	v_mul_f32_e32 v17, 0x3fb8aa3b, v17
	v_mul_f32_e32 v16, 0x3fb8aa3b, v16
	v_exp_f32_e32 v26, v17
	v_exp_f32_e32 v28, v16
	v_lshlrev_b32_e32 v16, 16, v55
	v_and_b32_e32 v17, 0xffff0000, v55
	v_pk_mul_f32 v[16:17], v[26:27], v[16:17] op_sel_hi:[0,1]
	v_pk_fma_f32 v[16:17], v[22:23], v[28:29], v[16:17] op_sel_hi:[1,0,1]
	v_pk_mul_f32 v[18:19], v[26:27], v[18:19] op_sel_hi:[0,1]
	v_pk_fma_f32 v[18:19], v[20:21], v[28:29], v[18:19] op_sel_hi:[1,0,1]
	v_bfe_u32 v20, v16, 16, 1
	v_add3_u32 v20, v16, v20, s11
	v_bfe_u32 v21, v17, 16, 1
	v_lshrrev_b32_e32 v20, 16, v20
	v_add3_u32 v21, v17, v21, s11
	v_and_or_b32 v22, v21, s24, v20
	v_add_co_u32_e32 v20, vcc, 0xffff8000, v6
	s_nop 1
	v_addc_co_u32_e32 v21, vcc, -1, v7, vcc
	global_store_dword v[20:21], v22, off
	s_and_saveexec_b64 s[22:23], s[2:3]
	s_cbranch_execz .LBB0_675
	v_add_co_u32_e32 v20, vcc, 0x1f901000, v10
	s_nop 1
	v_addc_co_u32_e32 v21, vcc, 0, v11, vcc
	global_store_dwordx2 v[20:21], v[18:19], off offset:3072

; __device__ __forceinline__ float bf_lo(unsigned w) { return __uint_as_float(w << 16); }
; __device__ __forceinline__ float bf_hi(unsigned w) { return __uint_as_float(w & 0xffff0000u); }
; __device__ __forceinline__ unsigned pk2(float lo, float hi) { return f2bf(lo) | (f2bf(hi) << 16); }
; __device__ __forceinline__ void p3_mlstm_scan(const Params& P, int tid, int vb) {
;     ...
;             for (int u = 0; u < 16; ++u) { const int item = bh * 256 + j0 + u;
;                 CS[(size_t)item * 8192 + idx] = pk2(C0, C1);
;                 if (hasn) *(float2*)(NS + (size_t)item * 128 + 2 * idx) = make_float2(n0, n1);
;                 if (idx == 0) SC[4096 + item] = m;
;                 const float mn = fmaxf(gg[u] + m, ml[u]), a = __expf(gg[u] + m - mn), bb = __expf(ml[u] - mn);
;                 C0 = a * C0 + bb * bf_lo(d[u]); C1 = a * C1 + bb * bf_hi(d[u]); n0 = a * n0 + bb * dn[u].x; n1 = a * n1 + bb * dn[u].y; m = mn; }
.LBB0_677:
	s_or_b64 exec, exec, s[22:23]
	s_waitcnt vmcnt(33)
	v_add_f32_e32 v21, v24, v56
	v_max_f32_e32 v20, v54, v54
	v_max_f32_e32 v20, v21, v20
	v_sub_f32_e32 v22, v54, v20
	v_sub_f32_e32 v21, v21, v20
	v_mul_f32_e32 v22, 0x3fb8aa3b, v22
	v_mul_f32_e32 v21, 0x3fb8aa3b, v21
	v_exp_f32_e32 v22, v22
	v_exp_f32_e32 v24, v21
	v_lshlrev_b32_e32 v26, 16, v51
	v_and_b32_e32 v27, 0xffff0000, v51
	v_pk_mul_f32 v[12:13], v[22:23], v[12:13] op_sel_hi:[0,1]
	v_pk_fma_f32 v[12:13], v[18:19], v[24:25], v[12:13] op_sel_hi:[1,0,1]
	v_pk_mul_f32 v[18:19], v[22:23], v[26:27] op_sel_hi:[0,1]
	v_pk_fma_f32 v[16:17], v[16:17], v[24:25], v[18:19] op_sel_hi:[1,0,1]
	s_nop 0
	v_and_b32_sdwa v19, v16, v49 dst_sel:DWORD dst_unused:UNUSED_PAD src0_sel:WORD_1 src1_sel:DWORD
	v_and_b32_sdwa v18, v17, v49 dst_sel:DWORD dst_unused:UNUSED_PAD src0_sel:WORD_1 src1_sel:DWORD
	v_add3_u32 v19, v16, v19, s11
	v_add3_u32 v18, v17, v18, s11
	v_lshrrev_b32_e32 v19, 16, v19
	v_and_or_b32 v18, v18, s24, v19
	global_store_dword v[6:7], v18, off
	s_and_saveexec_b64 s[22:23], s[2:3]
	s_cbranch_execz .LBB0_679
	v_add_co_u32_e32 v10, vcc, 0x1f901000, v10
	s_nop 1
	v_addc_co_u32_e32 v11, vcc, 0, v11, vcc
	global_store_dwordx2 v[10:11], v[12:13], off offset:3584
